# baseline (speedup 1.0000x reference)
_Z7k_attn3PKDF16_S0_PKiS2_PiPKDv8_DF16_PKfS6_S8_Pf:
	s_setprio 1
	s_mov_b32 s75, s2
	s_load_dwordx2 s[12:13], s[0:1], 0x8
	s_load_dwordx2 s[4:5], s[0:1], 0x18
	s_load_dwordx2 s[6:7], s[0:1], 0x28
	s_load_dwordx2 s[16:17], s[0:1], 0x10
	v_lshlrev_b32_e32 v13, 4, v0
	s_mul_i32 s3, s2, 0xc350
	v_or_b32_e32 v1, 0x4000, v13
	s_add_i32 s8, s3, 0xc350
	s_lshl_b32 s20, s2, 2
	s_waitcnt lgkmcnt(0)
	s_add_u32 s4, s4, s20
	s_addc_u32 s5, s5, 0
	s_load_dwordx2 s[18:19], s[4:5], 0x0
	global_load_dwordx4 v[100:103], v13, s[6:7]
	global_load_dwordx4 v[104:107], v1, s[6:7]
	v_or_b32_e32 v1, 0x8000, v13
	s_ashr_i32 s9, s8, 31
	v_or_b32_e32 v2, 0xc000, v13
	global_load_dwordx4 v[108:111], v1, s[6:7]
	global_load_dwordx4 v[112:115], v2, s[6:7]
	v_mov_b32_e32 v116, v13
	s_ashr_i32 s6, s3, 31
	s_lshr_b32 s9, s9, 24
	s_lshr_b32 s6, s6, 24
	s_add_i32 s8, s8, s9
	s_add_i32 s3, s3, s6
	v_lshrrev_b32_e32 v80, 6, v0
	s_ashr_i32 s8, s8, 8
	s_ashr_i32 s66, s3, 8
	s_sub_i32 s33, s8, s66
	v_lshlrev_b32_e32 v1, 1, v80
	v_and_b32_e32 v79, 15, v0
	s_add_i32 s67, s33, -1
	v_or_b32_e32 v11, 1, v1
	v_min_i32_e32 v12, s67, v1
	v_min_i32_e32 v10, s67, v11
	v_cmp_gt_u32_e64 s[38:39], 8, v79
	v_bfe_u32 v28, v0, 4, 2
	v_cmp_eq_u32_e32 vcc, 0, v0
	v_cndmask_b32_e64 v1, v10, v12, s[38:39]
	v_add_u32_e32 v2, s66, v1
	v_ashrrev_i32_e32 v3, 31, v2
	v_lshlrev_b64 v[2:3], 8, v[2:3]
	v_and_b32_e32 v1, 0x70, v13
	v_lshl_add_u64 v[8:9], s[12:13], 0, v[2:3]
	v_lshlrev_b32_e32 v2, 1, v1
	v_lshlrev_b32_e32 v1, 3, v28
	v_mov_b32_e32 v3, 0
	v_and_b32_e32 v22, 8, v1
	v_lshl_add_u64 v[8:9], v[8:9], 0, v[2:3]
	v_lshlrev_b32_e32 v26, 1, v22
	v_mov_b32_e32 v27, v3
	v_lshl_add_u64 v[8:9], v[8:9], 0, v[26:27]
	global_load_dwordx4 v[22:25], v[8:9], off nt
	s_and_saveexec_b64 s[6:7], vcc
	v_mov_b32_e32 v3, 16
	v_mov_b32_e32 v4, 0x26b40
	ds_write_b32 v4, v3
	s_or_b64 exec, exec, s[6:7]
	v_cmp_gt_u32_e32 vcc, 32, v0
	s_and_saveexec_b64 s[6:7], vcc
	v_mov_b32_e32 v3, 0x26d50
	v_lshl_add_u32 v3, v0, 2, v3
	v_mov_b32_e32 v4, 0
	ds_write_b32 v3, v4
	s_or_b64 exec, exec, s[6:7]
	s_movk_i32 s3, 0x100
	v_cmp_gt_u32_e32 vcc, s3, v0
	s_and_saveexec_b64 s[4:5], vcc
	v_mov_b32_e32 v3, 0x1dd00
	v_lshl_add_u32 v3, v0, 2, v3
	v_mov_b32_e32 v4, 0
	ds_write2st64_b32 v3, v4, v4 offset1:4
	s_or_b64 exec, exec, s[4:5]
	s_waitcnt lgkmcnt(0)
	s_add_i32 s76, s18, 3
	s_and_b32 s76, s76, -4
	s_mul_i32 s74, s75, 0x314
	s_add_i32 s76, s76, s74
	s_cmp_gt_i32 s19, s18
	s_cselect_b64 s[6:7], -1, 0
	s_add_i32 s24, s19, -1
	s_cmp_le_i32 s19, s18
	v_add_u32_e32 v3, s18, v0
	v_mov_b32_e32 v13, 0
	v_mov_b32_e32 v15, 0
	s_barrier
	s_cbranch_scc0 .LBB0_50
	v_cndmask_b32_e64 v4, 0, 1, s[6:7]
	v_cmp_ne_u32_e64 s[4:5], 1, v4
	s_andn2_b64 vcc, exec, s[6:7]
	s_cbranch_vccz .LBB0_51
